# diff tile loop head: K fragment ds_reads issued before the next tile's global loads (loop-edge reorder), on top of v048
# baseline (speedup 1.0000x reference)
.LBB0_1008:
	s_cmp_lt_u32 s10, s18
	s_cselect_b64 s[6:7], -1, 0
	s_add_i32 s8, s10, -1
	s_cmp_gt_u32 s8, s11
	s_cbranch_scc1 .Ldiff_nocomp
	s_bitcmp1_b32 s8, 0
	s_cselect_b32 s8, 0x9400, 0
	s_add_i32 s22, s8, 0
	v_add3_u32 v82, s22, v225, v239
	ds_read_b128 v[170:173], v82
	ds_read_b128 v[166:169], v82 offset:32
	ds_read_b128 v[174:177], v82 offset:8704
	ds_read_b128 v[158:161], v82 offset:8736
	ds_read_b128 v[154:157], v82 offset:64
	ds_read_b128 v[146:149], v82 offset:96
	ds_read_b128 v[162:165], v82 offset:8768
	ds_read_b128 v[150:153], v82 offset:8800
	s_andn2_b64 vcc, exec, s[6:7]
	s_cbranch_vccnz .Ldiff_noload
	v_add_co_u32_e32 v82, vcc, 0xfffcc000, v208
	s_nop 1
	v_addc_co_u32_e32 v83, vcc, -1, v209, vcc
	global_load_dwordx4 v[130:133], v[82:83], off offset:-1024
	global_load_dwordx4 v[134:137], v[82:83], off
	global_load_dwordx4 v[138:141], v[208:209], off offset:-1024
	global_load_dwordx4 v[142:145], v[208:209], off
.Ldiff_noload:
	s_cmp_le_u32 s21, s4
	s_mov_b64 s[8:9], -1
	s_cbranch_scc0 .LBB0_1014
	s_waitcnt lgkmcnt(7)
	v_mfma_f32_32x32x16_bf16 v[82:97], v[170:173], v[114:117], v[66:81]
	s_mov_b64 s[8:9], 0
	s_waitcnt lgkmcnt(5)
	v_mfma_f32_32x32x16_bf16 v[98:113], v[174:177], v[114:117], v[66:81]

.Ldiff_nocomp:
	s_andn2_b64 vcc, exec, s[6:7]
	s_cbranch_vccnz .LBB0_1007
	v_add_co_u32_e32 v82, vcc, 0xfffcc000, v208
	s_nop 1
	v_addc_co_u32_e32 v83, vcc, -1, v209, vcc
	global_load_dwordx4 v[130:133], v[82:83], off offset:-1024
	global_load_dwordx4 v[134:137], v[82:83], off
	global_load_dwordx4 v[138:141], v[208:209], off offset:-1024
	global_load_dwordx4 v[142:145], v[208:209], off
	s_branch .LBB0_1023
